# LoRA GEMM epilogue: iclr tiles skip the discarded decay exp (extra branch-free path per block)
# speedup vs baseline: 1.0061x; 1.0061x over previous
.LBB0_828:
	v_cndmask_b32_e64 v156, 0, 1, s[4:5]
	s_waitcnt vmcnt(0)
	v_pk_add_f32 v[136:137], v[136:137], v[112:113]
	v_pk_add_f32 v[134:135], v[134:135], v[110:111]
	v_pk_add_f32 v[132:133], v[132:133], v[108:109]
	v_cmp_ne_u32_e64 s[42:43], 1, v156
	s_andn2_b64 vcc, exec, s[4:5]
	v_pk_add_f32 v[130:131], v[130:131], v[106:107]
	s_cbranch_vccnz .LBB0_830
	s_and_b64 vcc, exec, s[40:41]
	s_cbranch_vccnz .Ldyn_dec_1
	v_mul_f32_e32 v134, 0xbfb8aa3b, v134
	v_mul_f32_e32 v130, 0xbfb8aa3b, v130
	v_exp_f32_e32 v134, v134
	v_exp_f32_e32 v130, v130
	v_mul_f32_e32 v135, 0xbfb8aa3b, v135
	v_mul_f32_e32 v131, 0xbfb8aa3b, v131
	v_add_f32_e32 v134, 1.0, v134
	v_add_f32_e32 v130, 1.0, v130
	v_rcp_f32_e32 v134, v134
	v_rcp_f32_e32 v130, v130
	v_exp_f32_e32 v135, v135
	v_exp_f32_e32 v131, v131
	v_add_f32_e32 v135, 1.0, v135
	v_add_f32_e32 v131, 1.0, v131
	v_mul_f32_e32 v136, 0xbfb8aa3b, v136
	v_mul_f32_e32 v132, 0xbfb8aa3b, v132
	v_rcp_f32_e32 v135, v135
	v_rcp_f32_e32 v131, v131
	v_exp_f32_e32 v136, v136
	v_exp_f32_e32 v132, v132
	v_add_f32_e32 v136, 1.0, v136
	v_add_f32_e32 v132, 1.0, v132
	v_mul_f32_e32 v137, 0xbfb8aa3b, v137
	v_mul_f32_e32 v133, 0xbfb8aa3b, v133
	v_rcp_f32_e32 v136, v136
	v_rcp_f32_e32 v132, v132
	v_exp_f32_e32 v137, v137
	v_exp_f32_e32 v133, v133
	v_add_f32_e32 v137, 1.0, v137
	v_add_f32_e32 v133, 1.0, v133
	v_rcp_f32_e32 v137, v137
	v_rcp_f32_e32 v133, v133
	s_branch .LBB0_830
.Ldyn_dec_1:
	v_mul_f32_e32 v134, 0xbfb8aa3b, v134
	v_mul_f32_e32 v130, 0xbfb8aa3b, v130
	v_exp_f32_e32 v134, v134
	v_exp_f32_e32 v130, v130
	v_mul_f32_e32 v135, 0xbfb8aa3b, v135
	v_mul_f32_e32 v131, 0xbfb8aa3b, v131
	v_add_f32_e32 v134, 1.0, v134
	v_add_f32_e32 v130, 1.0, v130
	v_rcp_f32_e32 v134, v134
	v_rcp_f32_e32 v130, v130
	v_exp_f32_e32 v135, v135
	v_exp_f32_e32 v131, v131
	v_mul_f32_e32 v156, 0xbf60028e, v134
	v_mul_f32_e32 v157, 0xbf60028e, v130
	v_add_f32_e32 v135, 1.0, v135
	v_add_f32_e32 v131, 1.0, v131
	v_mul_f32_e32 v136, 0xbfb8aa3b, v136
	v_mul_f32_e32 v132, 0xbfb8aa3b, v132
	v_exp_f32_e32 v156, v156
	v_exp_f32_e32 v157, v157
	v_rcp_f32_e32 v135, v135
	v_rcp_f32_e32 v131, v131
	v_exp_f32_e32 v136, v136
	v_exp_f32_e32 v132, v132
	v_cndmask_b32_e64 v134, v134, v156, s[40:41]
	v_cndmask_b32_e64 v130, v130, v157, s[40:41]
	v_mul_f32_e32 v156, 0xbf60028e, v135
	v_mul_f32_e32 v157, 0xbf60028e, v131
	v_add_f32_e32 v136, 1.0, v136
	v_add_f32_e32 v132, 1.0, v132
	v_mul_f32_e32 v137, 0xbfb8aa3b, v137
	v_mul_f32_e32 v133, 0xbfb8aa3b, v133
	v_exp_f32_e32 v156, v156
	v_exp_f32_e32 v157, v157
	v_rcp_f32_e32 v136, v136
	v_rcp_f32_e32 v132, v132
	v_exp_f32_e32 v137, v137
	v_exp_f32_e32 v133, v133
	v_cndmask_b32_e64 v135, v135, v156, s[40:41]
	v_cndmask_b32_e64 v131, v131, v157, s[40:41]
	v_mul_f32_e32 v156, 0xbf60028e, v136
	v_mul_f32_e32 v157, 0xbf60028e, v132
	v_add_f32_e32 v137, 1.0, v137
	v_add_f32_e32 v133, 1.0, v133
	v_exp_f32_e32 v156, v156
	v_exp_f32_e32 v157, v157
	v_rcp_f32_e32 v137, v137
	v_rcp_f32_e32 v133, v133
	v_cndmask_b32_e64 v136, v136, v156, s[40:41]
	v_cndmask_b32_e64 v132, v132, v157, s[40:41]
	v_mul_f32_e32 v156, 0xbf60028e, v137
	v_mul_f32_e32 v157, 0xbf60028e, v133
	v_exp_f32_e32 v156, v156
	v_exp_f32_e32 v157, v157
	v_cndmask_b32_e64 v137, v137, v156, s[40:41]
	v_cndmask_b32_e64 v133, v133, v157, s[40:41]
.LBB0_830:
	s_lshl_b32 s4, s70, 8
	s_add_i32 s4, s4, s20
	v_and_or_b32 v155, v155, 15, s4
	v_cvt_pk_bf16_f32 v134, v134, v135
	v_cvt_pk_bf16_f32 v135, v136, v137
	v_cvt_pk_bf16_f32 v136, v130, v131
	v_mov_b64_e32 v[130:131], s[50:51]
	v_mad_i64_i32 v[130:131], s[4:5], v155, s95, v[130:131]
	v_lshl_add_u64 v[130:131], v[150:151], 1, v[130:131]
	v_cvt_pk_bf16_f32 v137, v132, v133
	global_store_dwordx4 v[130:131], v[134:137], off sc1
	v_pk_add_f32 v[128:129], v[128:129], v[112:113]
	v_pk_add_f32 v[126:127], v[126:127], v[110:111]
	v_pk_add_f32 v[124:125], v[124:125], v[108:109]
	s_and_b64 vcc, exec, s[42:43]
	v_pk_add_f32 v[122:123], v[122:123], v[106:107]
	s_cbranch_vccnz .LBB0_832
	s_and_b64 vcc, exec, s[40:41]
	s_cbranch_vccnz .Ldyn_dec_2
	v_mul_f32_e32 v126, 0xbfb8aa3b, v126
	v_mul_f32_e32 v122, 0xbfb8aa3b, v122
	v_exp_f32_e32 v126, v126
	v_exp_f32_e32 v122, v122
	v_mul_f32_e32 v127, 0xbfb8aa3b, v127
	v_mul_f32_e32 v123, 0xbfb8aa3b, v123
	v_add_f32_e32 v126, 1.0, v126
	v_add_f32_e32 v122, 1.0, v122
	v_rcp_f32_e32 v126, v126
	v_rcp_f32_e32 v122, v122
	v_exp_f32_e32 v127, v127
	v_exp_f32_e32 v123, v123
	v_add_f32_e32 v127, 1.0, v127
	v_add_f32_e32 v123, 1.0, v123
	v_mul_f32_e32 v128, 0xbfb8aa3b, v128
	v_mul_f32_e32 v124, 0xbfb8aa3b, v124
	v_rcp_f32_e32 v127, v127
	v_rcp_f32_e32 v123, v123
	v_exp_f32_e32 v128, v128
	v_exp_f32_e32 v124, v124
	v_add_f32_e32 v128, 1.0, v128
	v_add_f32_e32 v124, 1.0, v124
	v_mul_f32_e32 v129, 0xbfb8aa3b, v129
	v_mul_f32_e32 v125, 0xbfb8aa3b, v125
	v_rcp_f32_e32 v128, v128
	v_rcp_f32_e32 v124, v124
	v_exp_f32_e32 v129, v129
	v_exp_f32_e32 v125, v125
	v_add_f32_e32 v129, 1.0, v129
	v_add_f32_e32 v125, 1.0, v125
	v_rcp_f32_e32 v129, v129
	v_rcp_f32_e32 v125, v125
	s_branch .LBB0_832
.Ldyn_dec_2:
	v_mul_f32_e32 v126, 0xbfb8aa3b, v126
	v_mul_f32_e32 v122, 0xbfb8aa3b, v122
	v_exp_f32_e32 v126, v126
	v_exp_f32_e32 v122, v122
	v_mul_f32_e32 v127, 0xbfb8aa3b, v127
	v_mul_f32_e32 v123, 0xbfb8aa3b, v123
	v_add_f32_e32 v126, 1.0, v126
	v_add_f32_e32 v122, 1.0, v122
	v_rcp_f32_e32 v126, v126
	v_rcp_f32_e32 v122, v122
	v_exp_f32_e32 v127, v127
	v_exp_f32_e32 v123, v123
	v_mul_f32_e32 v132, 0xbf60028e, v126
	v_mul_f32_e32 v133, 0xbf60028e, v122
	v_add_f32_e32 v127, 1.0, v127
	v_add_f32_e32 v123, 1.0, v123
	v_mul_f32_e32 v128, 0xbfb8aa3b, v128
	v_mul_f32_e32 v124, 0xbfb8aa3b, v124
	v_exp_f32_e32 v132, v132
	v_exp_f32_e32 v133, v133
	v_rcp_f32_e32 v127, v127
	v_rcp_f32_e32 v123, v123
	v_exp_f32_e32 v128, v128
	v_exp_f32_e32 v124, v124
	v_cndmask_b32_e64 v126, v126, v132, s[40:41]
	v_cndmask_b32_e64 v122, v122, v133, s[40:41]
	v_mul_f32_e32 v132, 0xbf60028e, v127
	v_mul_f32_e32 v133, 0xbf60028e, v123
	v_add_f32_e32 v128, 1.0, v128
	v_add_f32_e32 v124, 1.0, v124
	v_mul_f32_e32 v129, 0xbfb8aa3b, v129
	v_mul_f32_e32 v125, 0xbfb8aa3b, v125
	v_exp_f32_e32 v132, v132
	v_exp_f32_e32 v133, v133
	v_rcp_f32_e32 v128, v128
	v_rcp_f32_e32 v124, v124
	v_exp_f32_e32 v129, v129
	v_exp_f32_e32 v125, v125
	v_cndmask_b32_e64 v127, v127, v132, s[40:41]
	v_cndmask_b32_e64 v123, v123, v133, s[40:41]
	v_mul_f32_e32 v132, 0xbf60028e, v128
	v_mul_f32_e32 v133, 0xbf60028e, v124
	v_add_f32_e32 v129, 1.0, v129
	v_add_f32_e32 v125, 1.0, v125
	v_exp_f32_e32 v132, v132
	v_exp_f32_e32 v133, v133
	v_rcp_f32_e32 v129, v129
	v_rcp_f32_e32 v125, v125
	v_cndmask_b32_e64 v128, v128, v132, s[40:41]
	v_cndmask_b32_e64 v124, v124, v133, s[40:41]
	v_mul_f32_e32 v132, 0xbf60028e, v129
	v_mul_f32_e32 v133, 0xbf60028e, v125
	v_exp_f32_e32 v132, v132
	v_exp_f32_e32 v133, v133
	v_cndmask_b32_e64 v129, v129, v132, s[40:41]
	v_cndmask_b32_e64 v125, v125, v133, s[40:41]
.LBB0_832:
	v_cvt_pk_bf16_f32 v126, v126, v127
	v_cvt_pk_bf16_f32 v127, v128, v129
	v_cvt_pk_bf16_f32 v128, v122, v123
	v_cvt_pk_bf16_f32 v129, v124, v125
	v_or_b32_e32 v124, 16, v155
	v_mov_b64_e32 v[122:123], s[50:51]
	v_mad_i64_i32 v[122:123], s[4:5], v124, s95, v[122:123]
	v_lshl_add_u64 v[122:123], v[150:151], 1, v[122:123]
	global_store_dwordx4 v[122:123], v[126:129], off sc1
	v_pk_add_f32 v[120:121], v[120:121], v[112:113]
	v_pk_add_f32 v[118:119], v[118:119], v[110:111]
	v_pk_add_f32 v[116:117], v[116:117], v[108:109]
	s_and_b64 vcc, exec, s[42:43]
	v_pk_add_f32 v[114:115], v[114:115], v[106:107]
	s_cbranch_vccnz .LBB0_834
	s_and_b64 vcc, exec, s[40:41]
	s_cbranch_vccnz .Ldyn_dec_3
	v_mul_f32_e32 v118, 0xbfb8aa3b, v118
	v_mul_f32_e32 v114, 0xbfb8aa3b, v114
	v_exp_f32_e32 v118, v118
	v_exp_f32_e32 v114, v114
	v_mul_f32_e32 v119, 0xbfb8aa3b, v119
	v_mul_f32_e32 v115, 0xbfb8aa3b, v115
	v_add_f32_e32 v118, 1.0, v118
	v_add_f32_e32 v114, 1.0, v114
	v_rcp_f32_e32 v118, v118
	v_rcp_f32_e32 v114, v114
	v_exp_f32_e32 v119, v119
	v_exp_f32_e32 v115, v115
	v_add_f32_e32 v119, 1.0, v119
	v_add_f32_e32 v115, 1.0, v115
	v_mul_f32_e32 v120, 0xbfb8aa3b, v120
	v_mul_f32_e32 v116, 0xbfb8aa3b, v116
	v_rcp_f32_e32 v119, v119
	v_rcp_f32_e32 v115, v115
	v_exp_f32_e32 v120, v120
	v_exp_f32_e32 v116, v116
	v_add_f32_e32 v120, 1.0, v120
	v_add_f32_e32 v116, 1.0, v116
	v_mul_f32_e32 v121, 0xbfb8aa3b, v121
	v_mul_f32_e32 v117, 0xbfb8aa3b, v117
	v_rcp_f32_e32 v120, v120
	v_rcp_f32_e32 v116, v116
	v_exp_f32_e32 v121, v121
	v_exp_f32_e32 v117, v117
	v_add_f32_e32 v121, 1.0, v121
	v_add_f32_e32 v117, 1.0, v117
	v_rcp_f32_e32 v121, v121
	v_rcp_f32_e32 v117, v117
	s_branch .LBB0_834
.Ldyn_dec_3:
	v_mul_f32_e32 v118, 0xbfb8aa3b, v118
	v_mul_f32_e32 v114, 0xbfb8aa3b, v114
	v_exp_f32_e32 v118, v118
	v_exp_f32_e32 v114, v114
	v_mul_f32_e32 v119, 0xbfb8aa3b, v119
	v_mul_f32_e32 v115, 0xbfb8aa3b, v115
	v_add_f32_e32 v118, 1.0, v118
	v_add_f32_e32 v114, 1.0, v114
	v_rcp_f32_e32 v118, v118
	v_rcp_f32_e32 v114, v114
	v_exp_f32_e32 v119, v119
	v_exp_f32_e32 v115, v115
	v_mul_f32_e32 v124, 0xbf60028e, v118
	v_mul_f32_e32 v125, 0xbf60028e, v114
	v_add_f32_e32 v119, 1.0, v119
	v_add_f32_e32 v115, 1.0, v115
	v_mul_f32_e32 v120, 0xbfb8aa3b, v120
	v_mul_f32_e32 v116, 0xbfb8aa3b, v116
	v_exp_f32_e32 v124, v124
	v_exp_f32_e32 v125, v125
	v_rcp_f32_e32 v119, v119
	v_rcp_f32_e32 v115, v115
	v_exp_f32_e32 v120, v120
	v_exp_f32_e32 v116, v116
	v_cndmask_b32_e64 v118, v118, v124, s[40:41]
	v_cndmask_b32_e64 v114, v114, v125, s[40:41]
	v_mul_f32_e32 v124, 0xbf60028e, v119
	v_mul_f32_e32 v125, 0xbf60028e, v115
	v_add_f32_e32 v120, 1.0, v120
	v_add_f32_e32 v116, 1.0, v116
	v_mul_f32_e32 v121, 0xbfb8aa3b, v121
	v_mul_f32_e32 v117, 0xbfb8aa3b, v117
	v_exp_f32_e32 v124, v124
	v_exp_f32_e32 v125, v125
	v_rcp_f32_e32 v120, v120
	v_rcp_f32_e32 v116, v116
	v_exp_f32_e32 v121, v121
	v_exp_f32_e32 v117, v117
	v_cndmask_b32_e64 v119, v119, v124, s[40:41]
	v_cndmask_b32_e64 v115, v115, v125, s[40:41]
	v_mul_f32_e32 v124, 0xbf60028e, v120
	v_mul_f32_e32 v125, 0xbf60028e, v116
	v_add_f32_e32 v121, 1.0, v121
	v_add_f32_e32 v117, 1.0, v117
	v_exp_f32_e32 v124, v124
	v_exp_f32_e32 v125, v125
	v_rcp_f32_e32 v121, v121
	v_rcp_f32_e32 v117, v117
	v_cndmask_b32_e64 v120, v120, v124, s[40:41]
	v_cndmask_b32_e64 v116, v116, v125, s[40:41]
	v_mul_f32_e32 v124, 0xbf60028e, v121
	v_mul_f32_e32 v125, 0xbf60028e, v117
	v_exp_f32_e32 v124, v124
	v_exp_f32_e32 v125, v125
	v_cndmask_b32_e64 v121, v121, v124, s[40:41]
	v_cndmask_b32_e64 v117, v117, v125, s[40:41]
.LBB0_834:
	v_cvt_pk_bf16_f32 v118, v118, v119
	v_cvt_pk_bf16_f32 v119, v120, v121
	v_cvt_pk_bf16_f32 v120, v114, v115
	v_cvt_pk_bf16_f32 v121, v116, v117
	v_or_b32_e32 v116, 32, v155
	v_mov_b64_e32 v[114:115], s[50:51]
	v_mad_i64_i32 v[114:115], s[4:5], v116, s95, v[114:115]
	v_lshl_add_u64 v[114:115], v[150:151], 1, v[114:115]
	global_store_dwordx4 v[114:115], v[118:121], off sc1
	v_pk_add_f32 v[104:105], v[104:105], v[112:113]
	v_pk_add_f32 v[102:103], v[102:103], v[110:111]
	v_pk_add_f32 v[100:101], v[100:101], v[108:109]
	s_and_b64 vcc, exec, s[42:43]
	v_pk_add_f32 v[98:99], v[98:99], v[106:107]
	s_cbranch_vccnz .LBB0_836
	s_and_b64 vcc, exec, s[40:41]
	s_cbranch_vccnz .Ldyn_dec_4
	v_mul_f32_e32 v102, 0xbfb8aa3b, v102
	v_mul_f32_e32 v98, 0xbfb8aa3b, v98
	v_exp_f32_e32 v102, v102
	v_exp_f32_e32 v98, v98
	v_mul_f32_e32 v103, 0xbfb8aa3b, v103
	v_mul_f32_e32 v99, 0xbfb8aa3b, v99
	v_add_f32_e32 v102, 1.0, v102
	v_add_f32_e32 v98, 1.0, v98
	v_rcp_f32_e32 v102, v102
	v_rcp_f32_e32 v98, v98
	v_exp_f32_e32 v103, v103
	v_exp_f32_e32 v99, v99
	v_add_f32_e32 v103, 1.0, v103
	v_add_f32_e32 v99, 1.0, v99
	v_mul_f32_e32 v104, 0xbfb8aa3b, v104
	v_mul_f32_e32 v100, 0xbfb8aa3b, v100
	v_rcp_f32_e32 v103, v103
	v_rcp_f32_e32 v99, v99
	v_exp_f32_e32 v104, v104
	v_exp_f32_e32 v100, v100
	v_add_f32_e32 v104, 1.0, v104
	v_add_f32_e32 v100, 1.0, v100
	v_mul_f32_e32 v105, 0xbfb8aa3b, v105
	v_mul_f32_e32 v101, 0xbfb8aa3b, v101
	v_rcp_f32_e32 v104, v104
	v_rcp_f32_e32 v100, v100
	v_exp_f32_e32 v105, v105
	v_exp_f32_e32 v101, v101
	v_add_f32_e32 v105, 1.0, v105
	v_add_f32_e32 v101, 1.0, v101
	v_rcp_f32_e32 v105, v105
	v_rcp_f32_e32 v101, v101
	s_branch .LBB0_836
.Ldyn_dec_4:
	v_mul_f32_e32 v102, 0xbfb8aa3b, v102
	v_mul_f32_e32 v98, 0xbfb8aa3b, v98
	v_exp_f32_e32 v102, v102
	v_exp_f32_e32 v98, v98
	v_mul_f32_e32 v103, 0xbfb8aa3b, v103
	v_mul_f32_e32 v99, 0xbfb8aa3b, v99
	v_add_f32_e32 v102, 1.0, v102
	v_add_f32_e32 v98, 1.0, v98
	v_rcp_f32_e32 v102, v102
	v_rcp_f32_e32 v98, v98
	v_exp_f32_e32 v103, v103
	v_exp_f32_e32 v99, v99
	v_mul_f32_e32 v116, 0xbf60028e, v102
	v_mul_f32_e32 v117, 0xbf60028e, v98
	v_add_f32_e32 v103, 1.0, v103
	v_add_f32_e32 v99, 1.0, v99
	v_mul_f32_e32 v104, 0xbfb8aa3b, v104
	v_mul_f32_e32 v100, 0xbfb8aa3b, v100
	v_exp_f32_e32 v116, v116
	v_exp_f32_e32 v117, v117
	v_rcp_f32_e32 v103, v103
	v_rcp_f32_e32 v99, v99
	v_exp_f32_e32 v104, v104
	v_exp_f32_e32 v100, v100
	v_cndmask_b32_e64 v102, v102, v116, s[40:41]
	v_cndmask_b32_e64 v98, v98, v117, s[40:41]
	v_mul_f32_e32 v116, 0xbf60028e, v103
	v_mul_f32_e32 v117, 0xbf60028e, v99
	v_add_f32_e32 v104, 1.0, v104
	v_add_f32_e32 v100, 1.0, v100
	v_mul_f32_e32 v105, 0xbfb8aa3b, v105
	v_mul_f32_e32 v101, 0xbfb8aa3b, v101
	v_exp_f32_e32 v116, v116
	v_exp_f32_e32 v117, v117
	v_rcp_f32_e32 v104, v104
	v_rcp_f32_e32 v100, v100
	v_exp_f32_e32 v105, v105
	v_exp_f32_e32 v101, v101
	v_cndmask_b32_e64 v103, v103, v116, s[40:41]
	v_cndmask_b32_e64 v99, v99, v117, s[40:41]
	v_mul_f32_e32 v116, 0xbf60028e, v104
	v_mul_f32_e32 v117, 0xbf60028e, v100
	v_add_f32_e32 v105, 1.0, v105
	v_add_f32_e32 v101, 1.0, v101
	v_exp_f32_e32 v116, v116
	v_exp_f32_e32 v117, v117
	v_rcp_f32_e32 v105, v105
	v_rcp_f32_e32 v101, v101
	v_cndmask_b32_e64 v104, v104, v116, s[40:41]
	v_cndmask_b32_e64 v100, v100, v117, s[40:41]
	v_mul_f32_e32 v116, 0xbf60028e, v105
	v_mul_f32_e32 v117, 0xbf60028e, v101
	v_exp_f32_e32 v116, v116
	v_exp_f32_e32 v117, v117
	v_cndmask_b32_e64 v105, v105, v116, s[40:41]
	v_cndmask_b32_e64 v101, v101, v117, s[40:41]
.LBB0_836:
	v_cvt_pk_bf16_f32 v102, v102, v103
	v_cvt_pk_bf16_f32 v103, v104, v105
	v_cvt_pk_bf16_f32 v104, v98, v99
	v_cvt_pk_bf16_f32 v105, v100, v101
	v_or_b32_e32 v100, 48, v155
	v_mov_b64_e32 v[98:99], s[50:51]
	v_mad_i64_i32 v[98:99], s[4:5], v100, s95, v[98:99]
	v_lshl_add_u64 v[98:99], v[150:151], 1, v[98:99]
	global_store_dwordx4 v[98:99], v[102:105], off sc1
	v_pk_add_f32 v[96:97], v[96:97], v[112:113]
	v_pk_add_f32 v[94:95], v[94:95], v[110:111]
	v_pk_add_f32 v[92:93], v[92:93], v[108:109]
	s_and_b64 vcc, exec, s[42:43]
	v_pk_add_f32 v[90:91], v[90:91], v[106:107]
	s_cbranch_vccnz .LBB0_838
	s_and_b64 vcc, exec, s[40:41]
	s_cbranch_vccnz .Ldyn_dec_5
	v_mul_f32_e32 v94, 0xbfb8aa3b, v94
	v_mul_f32_e32 v90, 0xbfb8aa3b, v90
	v_exp_f32_e32 v94, v94
	v_exp_f32_e32 v90, v90
	v_mul_f32_e32 v95, 0xbfb8aa3b, v95
	v_mul_f32_e32 v91, 0xbfb8aa3b, v91
	v_add_f32_e32 v94, 1.0, v94
	v_add_f32_e32 v90, 1.0, v90
	v_rcp_f32_e32 v94, v94
	v_rcp_f32_e32 v90, v90
	v_exp_f32_e32 v95, v95
	v_exp_f32_e32 v91, v91
	v_add_f32_e32 v95, 1.0, v95
	v_add_f32_e32 v91, 1.0, v91
	v_mul_f32_e32 v96, 0xbfb8aa3b, v96
	v_mul_f32_e32 v92, 0xbfb8aa3b, v92
	v_rcp_f32_e32 v95, v95
	v_rcp_f32_e32 v91, v91
	v_exp_f32_e32 v96, v96
	v_exp_f32_e32 v92, v92
	v_add_f32_e32 v96, 1.0, v96
	v_add_f32_e32 v92, 1.0, v92
	v_mul_f32_e32 v97, 0xbfb8aa3b, v97
	v_mul_f32_e32 v93, 0xbfb8aa3b, v93
	v_rcp_f32_e32 v96, v96
	v_rcp_f32_e32 v92, v92
	v_exp_f32_e32 v97, v97
	v_exp_f32_e32 v93, v93
	v_add_f32_e32 v97, 1.0, v97
	v_add_f32_e32 v93, 1.0, v93
	v_rcp_f32_e32 v97, v97
	v_rcp_f32_e32 v93, v93
	s_branch .LBB0_838
.Ldyn_dec_5:
	v_mul_f32_e32 v94, 0xbfb8aa3b, v94
	v_mul_f32_e32 v90, 0xbfb8aa3b, v90
	v_exp_f32_e32 v94, v94
	v_exp_f32_e32 v90, v90
	v_mul_f32_e32 v95, 0xbfb8aa3b, v95
	v_mul_f32_e32 v91, 0xbfb8aa3b, v91
	v_add_f32_e32 v94, 1.0, v94
	v_add_f32_e32 v90, 1.0, v90
	v_rcp_f32_e32 v94, v94
	v_rcp_f32_e32 v90, v90
	v_exp_f32_e32 v95, v95
	v_exp_f32_e32 v91, v91
	v_mul_f32_e32 v100, 0xbf60028e, v94
	v_mul_f32_e32 v101, 0xbf60028e, v90
	v_add_f32_e32 v95, 1.0, v95
	v_add_f32_e32 v91, 1.0, v91
	v_mul_f32_e32 v96, 0xbfb8aa3b, v96
	v_mul_f32_e32 v92, 0xbfb8aa3b, v92
	v_exp_f32_e32 v100, v100
	v_exp_f32_e32 v101, v101
	v_rcp_f32_e32 v95, v95
	v_rcp_f32_e32 v91, v91
	v_exp_f32_e32 v96, v96
	v_exp_f32_e32 v92, v92
	v_cndmask_b32_e64 v94, v94, v100, s[40:41]
	v_cndmask_b32_e64 v90, v90, v101, s[40:41]
	v_mul_f32_e32 v100, 0xbf60028e, v95
	v_mul_f32_e32 v101, 0xbf60028e, v91
	v_add_f32_e32 v96, 1.0, v96
	v_add_f32_e32 v92, 1.0, v92
	v_mul_f32_e32 v97, 0xbfb8aa3b, v97
	v_mul_f32_e32 v93, 0xbfb8aa3b, v93
	v_exp_f32_e32 v100, v100
	v_exp_f32_e32 v101, v101
	v_rcp_f32_e32 v96, v96
	v_rcp_f32_e32 v92, v92
	v_exp_f32_e32 v97, v97
	v_exp_f32_e32 v93, v93
	v_cndmask_b32_e64 v95, v95, v100, s[40:41]
	v_cndmask_b32_e64 v91, v91, v101, s[40:41]
	v_mul_f32_e32 v100, 0xbf60028e, v96
	v_mul_f32_e32 v101, 0xbf60028e, v92
	v_add_f32_e32 v97, 1.0, v97
	v_add_f32_e32 v93, 1.0, v93
	v_exp_f32_e32 v100, v100
	v_exp_f32_e32 v101, v101
	v_rcp_f32_e32 v97, v97
	v_rcp_f32_e32 v93, v93
	v_cndmask_b32_e64 v96, v96, v100, s[40:41]
	v_cndmask_b32_e64 v92, v92, v101, s[40:41]
	v_mul_f32_e32 v100, 0xbf60028e, v97
	v_mul_f32_e32 v101, 0xbf60028e, v93
	v_exp_f32_e32 v100, v100
	v_exp_f32_e32 v101, v101
	v_cndmask_b32_e64 v97, v97, v100, s[40:41]
	v_cndmask_b32_e64 v93, v93, v101, s[40:41]
.LBB0_838:
	v_add_u32_e32 v100, 0x80, v155
	v_cvt_pk_bf16_f32 v94, v94, v95
	v_cvt_pk_bf16_f32 v95, v96, v97
	v_cvt_pk_bf16_f32 v96, v90, v91
	v_mov_b64_e32 v[90:91], s[50:51]
	v_mad_i64_i32 v[90:91], s[4:5], v100, s95, v[90:91]
	v_lshl_add_u64 v[90:91], v[150:151], 1, v[90:91]
	v_cvt_pk_bf16_f32 v97, v92, v93
	global_store_dwordx4 v[90:91], v[94:97], off sc1
	v_pk_add_f32 v[88:89], v[88:89], v[112:113]
	v_pk_add_f32 v[86:87], v[86:87], v[110:111]
	v_pk_add_f32 v[84:85], v[84:85], v[108:109]
	s_and_b64 vcc, exec, s[42:43]
	v_pk_add_f32 v[82:83], v[82:83], v[106:107]
	s_cbranch_vccnz .LBB0_840
	s_and_b64 vcc, exec, s[40:41]
	s_cbranch_vccnz .Ldyn_dec_6
	v_mul_f32_e32 v86, 0xbfb8aa3b, v86
	v_mul_f32_e32 v82, 0xbfb8aa3b, v82
	v_exp_f32_e32 v86, v86
	v_exp_f32_e32 v82, v82
	v_mul_f32_e32 v87, 0xbfb8aa3b, v87
	v_mul_f32_e32 v83, 0xbfb8aa3b, v83
	v_add_f32_e32 v86, 1.0, v86
	v_add_f32_e32 v82, 1.0, v82
	v_rcp_f32_e32 v86, v86
	v_rcp_f32_e32 v82, v82
	v_exp_f32_e32 v87, v87
	v_exp_f32_e32 v83, v83
	v_add_f32_e32 v87, 1.0, v87
	v_add_f32_e32 v83, 1.0, v83
	v_mul_f32_e32 v88, 0xbfb8aa3b, v88
	v_mul_f32_e32 v84, 0xbfb8aa3b, v84
	v_rcp_f32_e32 v87, v87
	v_rcp_f32_e32 v83, v83
	v_exp_f32_e32 v88, v88
	v_exp_f32_e32 v84, v84
	v_add_f32_e32 v88, 1.0, v88
	v_add_f32_e32 v84, 1.0, v84
	v_mul_f32_e32 v89, 0xbfb8aa3b, v89
	v_mul_f32_e32 v85, 0xbfb8aa3b, v85
	v_rcp_f32_e32 v88, v88
	v_rcp_f32_e32 v84, v84
	v_exp_f32_e32 v89, v89
	v_exp_f32_e32 v85, v85
	v_add_f32_e32 v89, 1.0, v89
	v_add_f32_e32 v85, 1.0, v85
	v_rcp_f32_e32 v89, v89
	v_rcp_f32_e32 v85, v85
	s_branch .LBB0_840
.Ldyn_dec_6:
	v_mul_f32_e32 v86, 0xbfb8aa3b, v86
	v_mul_f32_e32 v82, 0xbfb8aa3b, v82
	v_exp_f32_e32 v86, v86
	v_exp_f32_e32 v82, v82
	v_mul_f32_e32 v87, 0xbfb8aa3b, v87
	v_mul_f32_e32 v83, 0xbfb8aa3b, v83
	v_add_f32_e32 v86, 1.0, v86
	v_add_f32_e32 v82, 1.0, v82
	v_rcp_f32_e32 v86, v86
	v_rcp_f32_e32 v82, v82
	v_exp_f32_e32 v87, v87
	v_exp_f32_e32 v83, v83
	v_mul_f32_e32 v92, 0xbf60028e, v86
	v_mul_f32_e32 v93, 0xbf60028e, v82
	v_add_f32_e32 v87, 1.0, v87
	v_add_f32_e32 v83, 1.0, v83
	v_mul_f32_e32 v88, 0xbfb8aa3b, v88
	v_mul_f32_e32 v84, 0xbfb8aa3b, v84
	v_exp_f32_e32 v92, v92
	v_exp_f32_e32 v93, v93
	v_rcp_f32_e32 v87, v87
	v_rcp_f32_e32 v83, v83
	v_exp_f32_e32 v88, v88
	v_exp_f32_e32 v84, v84
	v_cndmask_b32_e64 v86, v86, v92, s[40:41]
	v_cndmask_b32_e64 v82, v82, v93, s[40:41]
	v_mul_f32_e32 v92, 0xbf60028e, v87
	v_mul_f32_e32 v93, 0xbf60028e, v83
	v_add_f32_e32 v88, 1.0, v88
	v_add_f32_e32 v84, 1.0, v84
	v_mul_f32_e32 v89, 0xbfb8aa3b, v89
	v_mul_f32_e32 v85, 0xbfb8aa3b, v85
	v_exp_f32_e32 v92, v92
	v_exp_f32_e32 v93, v93
	v_rcp_f32_e32 v88, v88
	v_rcp_f32_e32 v84, v84
	v_exp_f32_e32 v89, v89
	v_exp_f32_e32 v85, v85
	v_cndmask_b32_e64 v87, v87, v92, s[40:41]
	v_cndmask_b32_e64 v83, v83, v93, s[40:41]
	v_mul_f32_e32 v92, 0xbf60028e, v88
	v_mul_f32_e32 v93, 0xbf60028e, v84
	v_add_f32_e32 v89, 1.0, v89
	v_add_f32_e32 v85, 1.0, v85
	v_exp_f32_e32 v92, v92
	v_exp_f32_e32 v93, v93
	v_rcp_f32_e32 v89, v89
	v_rcp_f32_e32 v85, v85
	v_cndmask_b32_e64 v88, v88, v92, s[40:41]
	v_cndmask_b32_e64 v84, v84, v93, s[40:41]
	v_mul_f32_e32 v92, 0xbf60028e, v89
	v_mul_f32_e32 v93, 0xbf60028e, v85
	v_exp_f32_e32 v92, v92
	v_exp_f32_e32 v93, v93
	v_cndmask_b32_e64 v89, v89, v92, s[40:41]
	v_cndmask_b32_e64 v85, v85, v93, s[40:41]
.LBB0_840:
	v_cvt_pk_bf16_f32 v86, v86, v87
	v_cvt_pk_bf16_f32 v87, v88, v89
	v_cvt_pk_bf16_f32 v88, v82, v83
	v_cvt_pk_bf16_f32 v89, v84, v85
	v_add_u32_e32 v84, 0x90, v155
	v_mov_b64_e32 v[82:83], s[50:51]
	v_mad_i64_i32 v[82:83], s[4:5], v84, s95, v[82:83]
	v_lshl_add_u64 v[82:83], v[150:151], 1, v[82:83]
	global_store_dwordx4 v[82:83], v[86:89], off sc1
	v_pk_add_f32 v[80:81], v[80:81], v[112:113]
	v_pk_add_f32 v[78:79], v[78:79], v[110:111]
	v_pk_add_f32 v[76:77], v[76:77], v[108:109]
	s_and_b64 vcc, exec, s[42:43]
	v_pk_add_f32 v[74:75], v[74:75], v[106:107]
	s_cbranch_vccnz .LBB0_842
	s_and_b64 vcc, exec, s[40:41]
	s_cbranch_vccnz .Ldyn_dec_7
	v_mul_f32_e32 v78, 0xbfb8aa3b, v78
	v_mul_f32_e32 v74, 0xbfb8aa3b, v74
	v_exp_f32_e32 v78, v78
	v_exp_f32_e32 v74, v74
	v_mul_f32_e32 v79, 0xbfb8aa3b, v79
	v_mul_f32_e32 v75, 0xbfb8aa3b, v75
	v_add_f32_e32 v78, 1.0, v78
	v_add_f32_e32 v74, 1.0, v74
	v_rcp_f32_e32 v78, v78
	v_rcp_f32_e32 v74, v74
	v_exp_f32_e32 v79, v79
	v_exp_f32_e32 v75, v75
	v_add_f32_e32 v79, 1.0, v79
	v_add_f32_e32 v75, 1.0, v75
	v_mul_f32_e32 v80, 0xbfb8aa3b, v80
	v_mul_f32_e32 v76, 0xbfb8aa3b, v76
	v_rcp_f32_e32 v79, v79
	v_rcp_f32_e32 v75, v75
	v_exp_f32_e32 v80, v80
	v_exp_f32_e32 v76, v76
	v_add_f32_e32 v80, 1.0, v80
	v_add_f32_e32 v76, 1.0, v76
	v_mul_f32_e32 v81, 0xbfb8aa3b, v81
	v_mul_f32_e32 v77, 0xbfb8aa3b, v77
	v_rcp_f32_e32 v80, v80
	v_rcp_f32_e32 v76, v76
	v_exp_f32_e32 v81, v81
	v_exp_f32_e32 v77, v77
	v_add_f32_e32 v81, 1.0, v81
	v_add_f32_e32 v77, 1.0, v77
	v_rcp_f32_e32 v81, v81
	v_rcp_f32_e32 v77, v77
	s_branch .LBB0_842
.Ldyn_dec_7:
	v_mul_f32_e32 v78, 0xbfb8aa3b, v78
	v_mul_f32_e32 v74, 0xbfb8aa3b, v74
	v_exp_f32_e32 v78, v78
	v_exp_f32_e32 v74, v74
	v_mul_f32_e32 v79, 0xbfb8aa3b, v79
	v_mul_f32_e32 v75, 0xbfb8aa3b, v75
	v_add_f32_e32 v78, 1.0, v78
	v_add_f32_e32 v74, 1.0, v74
	v_rcp_f32_e32 v78, v78
	v_rcp_f32_e32 v74, v74
	v_exp_f32_e32 v79, v79
	v_exp_f32_e32 v75, v75
	v_mul_f32_e32 v84, 0xbf60028e, v78
	v_mul_f32_e32 v85, 0xbf60028e, v74
	v_add_f32_e32 v79, 1.0, v79
	v_add_f32_e32 v75, 1.0, v75
	v_mul_f32_e32 v80, 0xbfb8aa3b, v80
	v_mul_f32_e32 v76, 0xbfb8aa3b, v76
	v_exp_f32_e32 v84, v84
	v_exp_f32_e32 v85, v85
	v_rcp_f32_e32 v79, v79
	v_rcp_f32_e32 v75, v75
	v_exp_f32_e32 v80, v80
	v_exp_f32_e32 v76, v76
	v_cndmask_b32_e64 v78, v78, v84, s[40:41]
	v_cndmask_b32_e64 v74, v74, v85, s[40:41]
	v_mul_f32_e32 v84, 0xbf60028e, v79
	v_mul_f32_e32 v85, 0xbf60028e, v75
	v_add_f32_e32 v80, 1.0, v80
	v_add_f32_e32 v76, 1.0, v76
	v_mul_f32_e32 v81, 0xbfb8aa3b, v81
	v_mul_f32_e32 v77, 0xbfb8aa3b, v77
	v_exp_f32_e32 v84, v84
	v_exp_f32_e32 v85, v85
	v_rcp_f32_e32 v80, v80
	v_rcp_f32_e32 v76, v76
	v_exp_f32_e32 v81, v81
	v_exp_f32_e32 v77, v77
	v_cndmask_b32_e64 v79, v79, v84, s[40:41]
	v_cndmask_b32_e64 v75, v75, v85, s[40:41]
	v_mul_f32_e32 v84, 0xbf60028e, v80
	v_mul_f32_e32 v85, 0xbf60028e, v76
	v_add_f32_e32 v81, 1.0, v81
	v_add_f32_e32 v77, 1.0, v77
	v_exp_f32_e32 v84, v84
	v_exp_f32_e32 v85, v85
	v_rcp_f32_e32 v81, v81
	v_rcp_f32_e32 v77, v77
	v_cndmask_b32_e64 v80, v80, v84, s[40:41]
	v_cndmask_b32_e64 v76, v76, v85, s[40:41]
	v_mul_f32_e32 v84, 0xbf60028e, v81
	v_mul_f32_e32 v85, 0xbf60028e, v77
	v_exp_f32_e32 v84, v84
	v_exp_f32_e32 v85, v85
	v_cndmask_b32_e64 v81, v81, v84, s[40:41]
	v_cndmask_b32_e64 v77, v77, v85, s[40:41]
.LBB0_842:
	v_cvt_pk_bf16_f32 v78, v78, v79
	v_cvt_pk_bf16_f32 v79, v80, v81
	v_cvt_pk_bf16_f32 v80, v74, v75
	v_cvt_pk_bf16_f32 v81, v76, v77
	v_add_u32_e32 v76, 0xa0, v155
	v_mov_b64_e32 v[74:75], s[50:51]
	v_mad_i64_i32 v[74:75], s[4:5], v76, s95, v[74:75]
	v_lshl_add_u64 v[74:75], v[150:151], 1, v[74:75]
	global_store_dwordx4 v[74:75], v[78:81], off sc1
	v_pk_add_f32 v[72:73], v[72:73], v[112:113]
	v_pk_add_f32 v[70:71], v[70:71], v[110:111]
	v_pk_add_f32 v[68:69], v[68:69], v[108:109]
	s_and_b64 vcc, exec, s[42:43]
	v_pk_add_f32 v[66:67], v[66:67], v[106:107]
	s_cbranch_vccnz .LBB0_844
	s_and_b64 vcc, exec, s[40:41]
	s_cbranch_vccnz .Ldyn_dec_8
	v_mul_f32_e32 v70, 0xbfb8aa3b, v70
	v_mul_f32_e32 v66, 0xbfb8aa3b, v66
	v_exp_f32_e32 v70, v70
	v_exp_f32_e32 v66, v66
	v_mul_f32_e32 v71, 0xbfb8aa3b, v71
	v_mul_f32_e32 v67, 0xbfb8aa3b, v67
	v_add_f32_e32 v70, 1.0, v70
	v_add_f32_e32 v66, 1.0, v66
	v_rcp_f32_e32 v70, v70
	v_rcp_f32_e32 v66, v66
	v_exp_f32_e32 v71, v71
	v_exp_f32_e32 v67, v67
	v_add_f32_e32 v71, 1.0, v71
	v_add_f32_e32 v67, 1.0, v67
	v_mul_f32_e32 v72, 0xbfb8aa3b, v72
	v_mul_f32_e32 v68, 0xbfb8aa3b, v68
	v_rcp_f32_e32 v71, v71
	v_rcp_f32_e32 v67, v67
	v_exp_f32_e32 v72, v72
	v_exp_f32_e32 v68, v68
	v_add_f32_e32 v72, 1.0, v72
	v_add_f32_e32 v68, 1.0, v68
	v_mul_f32_e32 v73, 0xbfb8aa3b, v73
	v_mul_f32_e32 v69, 0xbfb8aa3b, v69
	v_rcp_f32_e32 v72, v72
	v_rcp_f32_e32 v68, v68
	v_exp_f32_e32 v73, v73
	v_exp_f32_e32 v69, v69
	v_add_f32_e32 v73, 1.0, v73
	v_add_f32_e32 v69, 1.0, v69
	v_rcp_f32_e32 v73, v73
	v_rcp_f32_e32 v69, v69
	s_branch .LBB0_844
.Ldyn_dec_8:
	v_mul_f32_e32 v70, 0xbfb8aa3b, v70
	v_mul_f32_e32 v66, 0xbfb8aa3b, v66
	v_exp_f32_e32 v70, v70
	v_exp_f32_e32 v66, v66
	v_mul_f32_e32 v71, 0xbfb8aa3b, v71
	v_mul_f32_e32 v67, 0xbfb8aa3b, v67
	v_add_f32_e32 v70, 1.0, v70
	v_add_f32_e32 v66, 1.0, v66
	v_rcp_f32_e32 v70, v70
	v_rcp_f32_e32 v66, v66
	v_exp_f32_e32 v71, v71
	v_exp_f32_e32 v67, v67
	v_mul_f32_e32 v76, 0xbf60028e, v70
	v_mul_f32_e32 v77, 0xbf60028e, v66
	v_add_f32_e32 v71, 1.0, v71
	v_add_f32_e32 v67, 1.0, v67
	v_mul_f32_e32 v72, 0xbfb8aa3b, v72
	v_mul_f32_e32 v68, 0xbfb8aa3b, v68
	v_exp_f32_e32 v76, v76
	v_exp_f32_e32 v77, v77
	v_rcp_f32_e32 v71, v71
	v_rcp_f32_e32 v67, v67
	v_exp_f32_e32 v72, v72
	v_exp_f32_e32 v68, v68
	v_cndmask_b32_e64 v70, v70, v76, s[40:41]
	v_cndmask_b32_e64 v66, v66, v77, s[40:41]
	v_mul_f32_e32 v76, 0xbf60028e, v71
	v_mul_f32_e32 v77, 0xbf60028e, v67
	v_add_f32_e32 v72, 1.0, v72
	v_add_f32_e32 v68, 1.0, v68
	v_mul_f32_e32 v73, 0xbfb8aa3b, v73
	v_mul_f32_e32 v69, 0xbfb8aa3b, v69
	v_exp_f32_e32 v76, v76
	v_exp_f32_e32 v77, v77
	v_rcp_f32_e32 v72, v72
	v_rcp_f32_e32 v68, v68
	v_exp_f32_e32 v73, v73
	v_exp_f32_e32 v69, v69
	v_cndmask_b32_e64 v71, v71, v76, s[40:41]
	v_cndmask_b32_e64 v67, v67, v77, s[40:41]
	v_mul_f32_e32 v76, 0xbf60028e, v72
	v_mul_f32_e32 v77, 0xbf60028e, v68
	v_add_f32_e32 v73, 1.0, v73
	v_add_f32_e32 v69, 1.0, v69
	v_exp_f32_e32 v76, v76
	v_exp_f32_e32 v77, v77
	v_rcp_f32_e32 v73, v73
	v_rcp_f32_e32 v69, v69
	v_cndmask_b32_e64 v72, v72, v76, s[40:41]
	v_cndmask_b32_e64 v68, v68, v77, s[40:41]
	v_mul_f32_e32 v76, 0xbf60028e, v73
	v_mul_f32_e32 v77, 0xbf60028e, v69
	v_exp_f32_e32 v76, v76
	v_exp_f32_e32 v77, v77
	v_cndmask_b32_e64 v73, v73, v76, s[40:41]
	v_cndmask_b32_e64 v69, v69, v77, s[40:41]

.LBB0_846:
	s_waitcnt vmcnt(0)
	v_pk_add_f32 v[64:65], v[64:65], v[72:73]
	v_pk_add_f32 v[62:63], v[62:63], v[70:71]
	v_pk_add_f32 v[60:61], v[60:61], v[68:69]
	s_and_b64 vcc, exec, s[42:43]
	v_pk_add_f32 v[58:59], v[58:59], v[66:67]
	s_cbranch_vccnz .LBB0_848
	s_and_b64 vcc, exec, s[40:41]
	s_cbranch_vccnz .Ldyn_dec_9
	v_mul_f32_e32 v62, 0xbfb8aa3b, v62
	v_mul_f32_e32 v58, 0xbfb8aa3b, v58
	v_exp_f32_e32 v62, v62
	v_exp_f32_e32 v58, v58
	v_mul_f32_e32 v63, 0xbfb8aa3b, v63
	v_mul_f32_e32 v59, 0xbfb8aa3b, v59
	v_add_f32_e32 v62, 1.0, v62
	v_add_f32_e32 v58, 1.0, v58
	v_rcp_f32_e32 v62, v62
	v_rcp_f32_e32 v58, v58
	v_exp_f32_e32 v63, v63
	v_exp_f32_e32 v59, v59
	v_add_f32_e32 v63, 1.0, v63
	v_add_f32_e32 v59, 1.0, v59
	v_mul_f32_e32 v64, 0xbfb8aa3b, v64
	v_mul_f32_e32 v60, 0xbfb8aa3b, v60
	v_rcp_f32_e32 v63, v63
	v_rcp_f32_e32 v59, v59
	v_exp_f32_e32 v64, v64
	v_exp_f32_e32 v60, v60
	v_add_f32_e32 v64, 1.0, v64
	v_add_f32_e32 v60, 1.0, v60
	v_mul_f32_e32 v65, 0xbfb8aa3b, v65
	v_mul_f32_e32 v61, 0xbfb8aa3b, v61
	v_rcp_f32_e32 v64, v64
	v_rcp_f32_e32 v60, v60
	v_exp_f32_e32 v65, v65
	v_exp_f32_e32 v61, v61
	v_add_f32_e32 v65, 1.0, v65
	v_add_f32_e32 v61, 1.0, v61
	v_rcp_f32_e32 v65, v65
	v_rcp_f32_e32 v61, v61
	s_branch .LBB0_848
.Ldyn_dec_9:
	v_mul_f32_e32 v62, 0xbfb8aa3b, v62
	v_mul_f32_e32 v58, 0xbfb8aa3b, v58
	v_exp_f32_e32 v62, v62
	v_exp_f32_e32 v58, v58
	v_mul_f32_e32 v63, 0xbfb8aa3b, v63
	v_mul_f32_e32 v59, 0xbfb8aa3b, v59
	v_add_f32_e32 v62, 1.0, v62
	v_add_f32_e32 v58, 1.0, v58
	v_rcp_f32_e32 v62, v62
	v_rcp_f32_e32 v58, v58
	v_exp_f32_e32 v63, v63
	v_exp_f32_e32 v59, v59
	v_mul_f32_e32 v78, 0xbf60028e, v62
	v_mul_f32_e32 v79, 0xbf60028e, v58
	v_add_f32_e32 v63, 1.0, v63
	v_add_f32_e32 v59, 1.0, v59
	v_mul_f32_e32 v64, 0xbfb8aa3b, v64
	v_mul_f32_e32 v60, 0xbfb8aa3b, v60
	v_exp_f32_e32 v78, v78
	v_exp_f32_e32 v79, v79
	v_rcp_f32_e32 v63, v63
	v_rcp_f32_e32 v59, v59
	v_exp_f32_e32 v64, v64
	v_exp_f32_e32 v60, v60
	v_cndmask_b32_e64 v62, v62, v78, s[40:41]
	v_cndmask_b32_e64 v58, v58, v79, s[40:41]
	v_mul_f32_e32 v78, 0xbf60028e, v63
	v_mul_f32_e32 v79, 0xbf60028e, v59
	v_add_f32_e32 v64, 1.0, v64
	v_add_f32_e32 v60, 1.0, v60
	v_mul_f32_e32 v65, 0xbfb8aa3b, v65
	v_mul_f32_e32 v61, 0xbfb8aa3b, v61
	v_exp_f32_e32 v78, v78
	v_exp_f32_e32 v79, v79
	v_rcp_f32_e32 v64, v64
	v_rcp_f32_e32 v60, v60
	v_exp_f32_e32 v65, v65
	v_exp_f32_e32 v61, v61
	v_cndmask_b32_e64 v63, v63, v78, s[40:41]
	v_cndmask_b32_e64 v59, v59, v79, s[40:41]
	v_mul_f32_e32 v78, 0xbf60028e, v64
	v_mul_f32_e32 v79, 0xbf60028e, v60
	v_add_f32_e32 v65, 1.0, v65
	v_add_f32_e32 v61, 1.0, v61
	v_exp_f32_e32 v78, v78
	v_exp_f32_e32 v79, v79
	v_rcp_f32_e32 v65, v65
	v_rcp_f32_e32 v61, v61
	v_cndmask_b32_e64 v64, v64, v78, s[40:41]
	v_cndmask_b32_e64 v60, v60, v79, s[40:41]
	v_mul_f32_e32 v78, 0xbf60028e, v65
	v_mul_f32_e32 v79, 0xbf60028e, v61
	v_exp_f32_e32 v78, v78
	v_exp_f32_e32 v79, v79
	v_cndmask_b32_e64 v65, v65, v78, s[40:41]
	v_cndmask_b32_e64 v61, v61, v79, s[40:41]
.LBB0_848:
	v_cvt_pk_bf16_f32 v62, v62, v63
	v_cvt_pk_bf16_f32 v63, v64, v65
	v_cvt_pk_bf16_f32 v64, v58, v59
	v_cvt_pk_bf16_f32 v65, v60, v61
	global_store_dwordx4 v[130:131], v[62:65], off offset:256 sc1
	v_pk_add_f32 v[56:57], v[56:57], v[72:73]
	v_pk_add_f32 v[54:55], v[54:55], v[70:71]
	v_pk_add_f32 v[52:53], v[52:53], v[68:69]
	s_and_b64 vcc, exec, s[42:43]
	v_pk_add_f32 v[50:51], v[50:51], v[66:67]
	s_cbranch_vccnz .LBB0_850
	s_and_b64 vcc, exec, s[40:41]
	s_cbranch_vccnz .Ldyn_dec_10
	v_mul_f32_e32 v54, 0xbfb8aa3b, v54
	v_mul_f32_e32 v50, 0xbfb8aa3b, v50
	v_exp_f32_e32 v54, v54
	v_exp_f32_e32 v50, v50
	v_mul_f32_e32 v55, 0xbfb8aa3b, v55
	v_mul_f32_e32 v51, 0xbfb8aa3b, v51
	v_add_f32_e32 v54, 1.0, v54
	v_add_f32_e32 v50, 1.0, v50
	v_rcp_f32_e32 v54, v54
	v_rcp_f32_e32 v50, v50
	v_exp_f32_e32 v55, v55
	v_exp_f32_e32 v51, v51
	v_add_f32_e32 v55, 1.0, v55
	v_add_f32_e32 v51, 1.0, v51
	v_mul_f32_e32 v56, 0xbfb8aa3b, v56
	v_mul_f32_e32 v52, 0xbfb8aa3b, v52
	v_rcp_f32_e32 v55, v55
	v_rcp_f32_e32 v51, v51
	v_exp_f32_e32 v56, v56
	v_exp_f32_e32 v52, v52
	v_add_f32_e32 v56, 1.0, v56
	v_add_f32_e32 v52, 1.0, v52
	v_mul_f32_e32 v57, 0xbfb8aa3b, v57
	v_mul_f32_e32 v53, 0xbfb8aa3b, v53
	v_rcp_f32_e32 v56, v56
	v_rcp_f32_e32 v52, v52
	v_exp_f32_e32 v57, v57
	v_exp_f32_e32 v53, v53
	v_add_f32_e32 v57, 1.0, v57
	v_add_f32_e32 v53, 1.0, v53
	v_rcp_f32_e32 v57, v57
	v_rcp_f32_e32 v53, v53
	s_branch .LBB0_850
.Ldyn_dec_10:
	v_mul_f32_e32 v54, 0xbfb8aa3b, v54
	v_mul_f32_e32 v50, 0xbfb8aa3b, v50
	v_exp_f32_e32 v54, v54
	v_exp_f32_e32 v50, v50
	v_mul_f32_e32 v55, 0xbfb8aa3b, v55
	v_mul_f32_e32 v51, 0xbfb8aa3b, v51
	v_add_f32_e32 v54, 1.0, v54
	v_add_f32_e32 v50, 1.0, v50
	v_rcp_f32_e32 v54, v54
	v_rcp_f32_e32 v50, v50
	v_exp_f32_e32 v55, v55
	v_exp_f32_e32 v51, v51
	v_mul_f32_e32 v58, 0xbf60028e, v54
	v_mul_f32_e32 v59, 0xbf60028e, v50
	v_add_f32_e32 v55, 1.0, v55
	v_add_f32_e32 v51, 1.0, v51
	v_mul_f32_e32 v56, 0xbfb8aa3b, v56
	v_mul_f32_e32 v52, 0xbfb8aa3b, v52
	v_exp_f32_e32 v58, v58
	v_exp_f32_e32 v59, v59
	v_rcp_f32_e32 v55, v55
	v_rcp_f32_e32 v51, v51
	v_exp_f32_e32 v56, v56
	v_exp_f32_e32 v52, v52
	v_cndmask_b32_e64 v54, v54, v58, s[40:41]
	v_cndmask_b32_e64 v50, v50, v59, s[40:41]
	v_mul_f32_e32 v58, 0xbf60028e, v55
	v_mul_f32_e32 v59, 0xbf60028e, v51
	v_add_f32_e32 v56, 1.0, v56
	v_add_f32_e32 v52, 1.0, v52
	v_mul_f32_e32 v57, 0xbfb8aa3b, v57
	v_mul_f32_e32 v53, 0xbfb8aa3b, v53
	v_exp_f32_e32 v58, v58
	v_exp_f32_e32 v59, v59
	v_rcp_f32_e32 v56, v56
	v_rcp_f32_e32 v52, v52
	v_exp_f32_e32 v57, v57
	v_exp_f32_e32 v53, v53
	v_cndmask_b32_e64 v55, v55, v58, s[40:41]
	v_cndmask_b32_e64 v51, v51, v59, s[40:41]
	v_mul_f32_e32 v58, 0xbf60028e, v56
	v_mul_f32_e32 v59, 0xbf60028e, v52
	v_add_f32_e32 v57, 1.0, v57
	v_add_f32_e32 v53, 1.0, v53
	v_exp_f32_e32 v58, v58
	v_exp_f32_e32 v59, v59
	v_rcp_f32_e32 v57, v57
	v_rcp_f32_e32 v53, v53
	v_cndmask_b32_e64 v56, v56, v58, s[40:41]
	v_cndmask_b32_e64 v52, v52, v59, s[40:41]
	v_mul_f32_e32 v58, 0xbf60028e, v57
	v_mul_f32_e32 v59, 0xbf60028e, v53
	v_exp_f32_e32 v58, v58
	v_exp_f32_e32 v59, v59
	v_cndmask_b32_e64 v57, v57, v58, s[40:41]
	v_cndmask_b32_e64 v53, v53, v59, s[40:41]
.LBB0_850:
	v_cvt_pk_bf16_f32 v54, v54, v55
	v_cvt_pk_bf16_f32 v55, v56, v57
	v_cvt_pk_bf16_f32 v56, v50, v51
	v_cvt_pk_bf16_f32 v57, v52, v53
	global_store_dwordx4 v[122:123], v[54:57], off offset:256 sc1
	v_pk_add_f32 v[48:49], v[48:49], v[72:73]
	v_pk_add_f32 v[46:47], v[46:47], v[70:71]
	v_pk_add_f32 v[44:45], v[44:45], v[68:69]
	s_and_b64 vcc, exec, s[42:43]
	v_pk_add_f32 v[42:43], v[42:43], v[66:67]
	s_cbranch_vccnz .LBB0_852
	s_and_b64 vcc, exec, s[40:41]
	s_cbranch_vccnz .Ldyn_dec_11
	v_mul_f32_e32 v46, 0xbfb8aa3b, v46
	v_mul_f32_e32 v42, 0xbfb8aa3b, v42
	v_exp_f32_e32 v46, v46
	v_exp_f32_e32 v42, v42
	v_mul_f32_e32 v47, 0xbfb8aa3b, v47
	v_mul_f32_e32 v43, 0xbfb8aa3b, v43
	v_add_f32_e32 v46, 1.0, v46
	v_add_f32_e32 v42, 1.0, v42
	v_rcp_f32_e32 v46, v46
	v_rcp_f32_e32 v42, v42
	v_exp_f32_e32 v47, v47
	v_exp_f32_e32 v43, v43
	v_add_f32_e32 v47, 1.0, v47
	v_add_f32_e32 v43, 1.0, v43
	v_mul_f32_e32 v48, 0xbfb8aa3b, v48
	v_mul_f32_e32 v44, 0xbfb8aa3b, v44
	v_rcp_f32_e32 v47, v47
	v_rcp_f32_e32 v43, v43
	v_exp_f32_e32 v48, v48
	v_exp_f32_e32 v44, v44
	v_add_f32_e32 v48, 1.0, v48
	v_add_f32_e32 v44, 1.0, v44
	v_mul_f32_e32 v49, 0xbfb8aa3b, v49
	v_mul_f32_e32 v45, 0xbfb8aa3b, v45
	v_rcp_f32_e32 v48, v48
	v_rcp_f32_e32 v44, v44
	v_exp_f32_e32 v49, v49
	v_exp_f32_e32 v45, v45
	v_add_f32_e32 v49, 1.0, v49
	v_add_f32_e32 v45, 1.0, v45
	v_rcp_f32_e32 v49, v49
	v_rcp_f32_e32 v45, v45
	s_branch .LBB0_852
.Ldyn_dec_11:
	v_mul_f32_e32 v46, 0xbfb8aa3b, v46
	v_mul_f32_e32 v42, 0xbfb8aa3b, v42
	v_exp_f32_e32 v46, v46
	v_exp_f32_e32 v42, v42
	v_mul_f32_e32 v47, 0xbfb8aa3b, v47
	v_mul_f32_e32 v43, 0xbfb8aa3b, v43
	v_add_f32_e32 v46, 1.0, v46
	v_add_f32_e32 v42, 1.0, v42
	v_rcp_f32_e32 v46, v46
	v_rcp_f32_e32 v42, v42
	v_exp_f32_e32 v47, v47
	v_exp_f32_e32 v43, v43
	v_mul_f32_e32 v50, 0xbf60028e, v46
	v_mul_f32_e32 v51, 0xbf60028e, v42
	v_add_f32_e32 v47, 1.0, v47
	v_add_f32_e32 v43, 1.0, v43
	v_mul_f32_e32 v48, 0xbfb8aa3b, v48
	v_mul_f32_e32 v44, 0xbfb8aa3b, v44
	v_exp_f32_e32 v50, v50
	v_exp_f32_e32 v51, v51
	v_rcp_f32_e32 v47, v47
	v_rcp_f32_e32 v43, v43
	v_exp_f32_e32 v48, v48
	v_exp_f32_e32 v44, v44
	v_cndmask_b32_e64 v46, v46, v50, s[40:41]
	v_cndmask_b32_e64 v42, v42, v51, s[40:41]
	v_mul_f32_e32 v50, 0xbf60028e, v47
	v_mul_f32_e32 v51, 0xbf60028e, v43
	v_add_f32_e32 v48, 1.0, v48
	v_add_f32_e32 v44, 1.0, v44
	v_mul_f32_e32 v49, 0xbfb8aa3b, v49
	v_mul_f32_e32 v45, 0xbfb8aa3b, v45
	v_exp_f32_e32 v50, v50
	v_exp_f32_e32 v51, v51
	v_rcp_f32_e32 v48, v48
	v_rcp_f32_e32 v44, v44
	v_exp_f32_e32 v49, v49
	v_exp_f32_e32 v45, v45
	v_cndmask_b32_e64 v47, v47, v50, s[40:41]
	v_cndmask_b32_e64 v43, v43, v51, s[40:41]
	v_mul_f32_e32 v50, 0xbf60028e, v48
	v_mul_f32_e32 v51, 0xbf60028e, v44
	v_add_f32_e32 v49, 1.0, v49
	v_add_f32_e32 v45, 1.0, v45
	v_exp_f32_e32 v50, v50
	v_exp_f32_e32 v51, v51
	v_rcp_f32_e32 v49, v49
	v_rcp_f32_e32 v45, v45
	v_cndmask_b32_e64 v48, v48, v50, s[40:41]
	v_cndmask_b32_e64 v44, v44, v51, s[40:41]
	v_mul_f32_e32 v50, 0xbf60028e, v49
	v_mul_f32_e32 v51, 0xbf60028e, v45
	v_exp_f32_e32 v50, v50
	v_exp_f32_e32 v51, v51
	v_cndmask_b32_e64 v49, v49, v50, s[40:41]
	v_cndmask_b32_e64 v45, v45, v51, s[40:41]
.LBB0_852:
	v_cvt_pk_bf16_f32 v46, v46, v47
	v_cvt_pk_bf16_f32 v47, v48, v49
	v_cvt_pk_bf16_f32 v48, v42, v43
	v_cvt_pk_bf16_f32 v49, v44, v45
	global_store_dwordx4 v[114:115], v[46:49], off offset:256 sc1
	v_pk_add_f32 v[40:41], v[40:41], v[72:73]
	v_pk_add_f32 v[38:39], v[38:39], v[70:71]
	v_pk_add_f32 v[36:37], v[36:37], v[68:69]
	s_and_b64 vcc, exec, s[42:43]
	v_pk_add_f32 v[34:35], v[34:35], v[66:67]
	s_cbranch_vccnz .LBB0_854
	s_and_b64 vcc, exec, s[40:41]
	s_cbranch_vccnz .Ldyn_dec_12
	v_mul_f32_e32 v38, 0xbfb8aa3b, v38
	v_mul_f32_e32 v34, 0xbfb8aa3b, v34
	v_exp_f32_e32 v38, v38
	v_exp_f32_e32 v34, v34
	v_mul_f32_e32 v39, 0xbfb8aa3b, v39
	v_mul_f32_e32 v35, 0xbfb8aa3b, v35
	v_add_f32_e32 v38, 1.0, v38
	v_add_f32_e32 v34, 1.0, v34
	v_rcp_f32_e32 v38, v38
	v_rcp_f32_e32 v34, v34
	v_exp_f32_e32 v39, v39
	v_exp_f32_e32 v35, v35
	v_add_f32_e32 v39, 1.0, v39
	v_add_f32_e32 v35, 1.0, v35
	v_mul_f32_e32 v40, 0xbfb8aa3b, v40
	v_mul_f32_e32 v36, 0xbfb8aa3b, v36
	v_rcp_f32_e32 v39, v39
	v_rcp_f32_e32 v35, v35
	v_exp_f32_e32 v40, v40
	v_exp_f32_e32 v36, v36
	v_add_f32_e32 v40, 1.0, v40
	v_add_f32_e32 v36, 1.0, v36
	v_mul_f32_e32 v41, 0xbfb8aa3b, v41
	v_mul_f32_e32 v37, 0xbfb8aa3b, v37
	v_rcp_f32_e32 v40, v40
	v_rcp_f32_e32 v36, v36
	v_exp_f32_e32 v41, v41
	v_exp_f32_e32 v37, v37
	v_add_f32_e32 v41, 1.0, v41
	v_add_f32_e32 v37, 1.0, v37
	v_rcp_f32_e32 v41, v41
	v_rcp_f32_e32 v37, v37
	s_branch .LBB0_854
.Ldyn_dec_12:
	v_mul_f32_e32 v38, 0xbfb8aa3b, v38
	v_mul_f32_e32 v34, 0xbfb8aa3b, v34
	v_exp_f32_e32 v38, v38
	v_exp_f32_e32 v34, v34
	v_mul_f32_e32 v39, 0xbfb8aa3b, v39
	v_mul_f32_e32 v35, 0xbfb8aa3b, v35
	v_add_f32_e32 v38, 1.0, v38
	v_add_f32_e32 v34, 1.0, v34
	v_rcp_f32_e32 v38, v38
	v_rcp_f32_e32 v34, v34
	v_exp_f32_e32 v39, v39
	v_exp_f32_e32 v35, v35
	v_mul_f32_e32 v42, 0xbf60028e, v38
	v_mul_f32_e32 v43, 0xbf60028e, v34
	v_add_f32_e32 v39, 1.0, v39
	v_add_f32_e32 v35, 1.0, v35
	v_mul_f32_e32 v40, 0xbfb8aa3b, v40
	v_mul_f32_e32 v36, 0xbfb8aa3b, v36
	v_exp_f32_e32 v42, v42
	v_exp_f32_e32 v43, v43
	v_rcp_f32_e32 v39, v39
	v_rcp_f32_e32 v35, v35
	v_exp_f32_e32 v40, v40
	v_exp_f32_e32 v36, v36
	v_cndmask_b32_e64 v38, v38, v42, s[40:41]
	v_cndmask_b32_e64 v34, v34, v43, s[40:41]
	v_mul_f32_e32 v42, 0xbf60028e, v39
	v_mul_f32_e32 v43, 0xbf60028e, v35
	v_add_f32_e32 v40, 1.0, v40
	v_add_f32_e32 v36, 1.0, v36
	v_mul_f32_e32 v41, 0xbfb8aa3b, v41
	v_mul_f32_e32 v37, 0xbfb8aa3b, v37
	v_exp_f32_e32 v42, v42
	v_exp_f32_e32 v43, v43
	v_rcp_f32_e32 v40, v40
	v_rcp_f32_e32 v36, v36
	v_exp_f32_e32 v41, v41
	v_exp_f32_e32 v37, v37
	v_cndmask_b32_e64 v39, v39, v42, s[40:41]
	v_cndmask_b32_e64 v35, v35, v43, s[40:41]
	v_mul_f32_e32 v42, 0xbf60028e, v40
	v_mul_f32_e32 v43, 0xbf60028e, v36
	v_add_f32_e32 v41, 1.0, v41
	v_add_f32_e32 v37, 1.0, v37
	v_exp_f32_e32 v42, v42
	v_exp_f32_e32 v43, v43
	v_rcp_f32_e32 v41, v41
	v_rcp_f32_e32 v37, v37
	v_cndmask_b32_e64 v40, v40, v42, s[40:41]
	v_cndmask_b32_e64 v36, v36, v43, s[40:41]
	v_mul_f32_e32 v42, 0xbf60028e, v41
	v_mul_f32_e32 v43, 0xbf60028e, v37
	v_exp_f32_e32 v42, v42
	v_exp_f32_e32 v43, v43
	v_cndmask_b32_e64 v41, v41, v42, s[40:41]
	v_cndmask_b32_e64 v37, v37, v43, s[40:41]
.LBB0_854:
	v_cvt_pk_bf16_f32 v38, v38, v39
	v_cvt_pk_bf16_f32 v39, v40, v41
	v_cvt_pk_bf16_f32 v40, v34, v35
	v_cvt_pk_bf16_f32 v41, v36, v37
	global_store_dwordx4 v[98:99], v[38:41], off offset:256 sc1
	v_pk_add_f32 v[32:33], v[32:33], v[72:73]
	v_pk_add_f32 v[30:31], v[30:31], v[70:71]
	v_pk_add_f32 v[28:29], v[28:29], v[68:69]
	s_and_b64 vcc, exec, s[42:43]
	v_pk_add_f32 v[26:27], v[26:27], v[66:67]
	s_cbranch_vccnz .LBB0_856
	s_and_b64 vcc, exec, s[40:41]
	s_cbranch_vccnz .Ldyn_dec_13
	v_mul_f32_e32 v30, 0xbfb8aa3b, v30
	v_mul_f32_e32 v26, 0xbfb8aa3b, v26
	v_exp_f32_e32 v30, v30
	v_exp_f32_e32 v26, v26
	v_mul_f32_e32 v31, 0xbfb8aa3b, v31
	v_mul_f32_e32 v27, 0xbfb8aa3b, v27
	v_add_f32_e32 v30, 1.0, v30
	v_add_f32_e32 v26, 1.0, v26
	v_rcp_f32_e32 v30, v30
	v_rcp_f32_e32 v26, v26
	v_exp_f32_e32 v31, v31
	v_exp_f32_e32 v27, v27
	v_add_f32_e32 v31, 1.0, v31
	v_add_f32_e32 v27, 1.0, v27
	v_mul_f32_e32 v32, 0xbfb8aa3b, v32
	v_mul_f32_e32 v28, 0xbfb8aa3b, v28
	v_rcp_f32_e32 v31, v31
	v_rcp_f32_e32 v27, v27
	v_exp_f32_e32 v32, v32
	v_exp_f32_e32 v28, v28
	v_add_f32_e32 v32, 1.0, v32
	v_add_f32_e32 v28, 1.0, v28
	v_mul_f32_e32 v33, 0xbfb8aa3b, v33
	v_mul_f32_e32 v29, 0xbfb8aa3b, v29
	v_rcp_f32_e32 v32, v32
	v_rcp_f32_e32 v28, v28
	v_exp_f32_e32 v33, v33
	v_exp_f32_e32 v29, v29
	v_add_f32_e32 v33, 1.0, v33
	v_add_f32_e32 v29, 1.0, v29
	v_rcp_f32_e32 v33, v33
	v_rcp_f32_e32 v29, v29
	s_branch .LBB0_856
.Ldyn_dec_13:
	v_mul_f32_e32 v30, 0xbfb8aa3b, v30
	v_mul_f32_e32 v26, 0xbfb8aa3b, v26
	v_exp_f32_e32 v30, v30
	v_exp_f32_e32 v26, v26
	v_mul_f32_e32 v31, 0xbfb8aa3b, v31
	v_mul_f32_e32 v27, 0xbfb8aa3b, v27
	v_add_f32_e32 v30, 1.0, v30
	v_add_f32_e32 v26, 1.0, v26
	v_rcp_f32_e32 v30, v30
	v_rcp_f32_e32 v26, v26
	v_exp_f32_e32 v31, v31
	v_exp_f32_e32 v27, v27
	v_mul_f32_e32 v34, 0xbf60028e, v30
	v_mul_f32_e32 v35, 0xbf60028e, v26
	v_add_f32_e32 v31, 1.0, v31
	v_add_f32_e32 v27, 1.0, v27
	v_mul_f32_e32 v32, 0xbfb8aa3b, v32
	v_mul_f32_e32 v28, 0xbfb8aa3b, v28
	v_exp_f32_e32 v34, v34
	v_exp_f32_e32 v35, v35
	v_rcp_f32_e32 v31, v31
	v_rcp_f32_e32 v27, v27
	v_exp_f32_e32 v32, v32
	v_exp_f32_e32 v28, v28
	v_cndmask_b32_e64 v30, v30, v34, s[40:41]
	v_cndmask_b32_e64 v26, v26, v35, s[40:41]
	v_mul_f32_e32 v34, 0xbf60028e, v31
	v_mul_f32_e32 v35, 0xbf60028e, v27
	v_add_f32_e32 v32, 1.0, v32
	v_add_f32_e32 v28, 1.0, v28
	v_mul_f32_e32 v33, 0xbfb8aa3b, v33
	v_mul_f32_e32 v29, 0xbfb8aa3b, v29
	v_exp_f32_e32 v34, v34
	v_exp_f32_e32 v35, v35
	v_rcp_f32_e32 v32, v32
	v_rcp_f32_e32 v28, v28
	v_exp_f32_e32 v33, v33
	v_exp_f32_e32 v29, v29
	v_cndmask_b32_e64 v31, v31, v34, s[40:41]
	v_cndmask_b32_e64 v27, v27, v35, s[40:41]
	v_mul_f32_e32 v34, 0xbf60028e, v32
	v_mul_f32_e32 v35, 0xbf60028e, v28
	v_add_f32_e32 v33, 1.0, v33
	v_add_f32_e32 v29, 1.0, v29
	v_exp_f32_e32 v34, v34
	v_exp_f32_e32 v35, v35
	v_rcp_f32_e32 v33, v33
	v_rcp_f32_e32 v29, v29
	v_cndmask_b32_e64 v32, v32, v34, s[40:41]
	v_cndmask_b32_e64 v28, v28, v35, s[40:41]
	v_mul_f32_e32 v34, 0xbf60028e, v33
	v_mul_f32_e32 v35, 0xbf60028e, v29
	v_exp_f32_e32 v34, v34
	v_exp_f32_e32 v35, v35
	v_cndmask_b32_e64 v33, v33, v34, s[40:41]
	v_cndmask_b32_e64 v29, v29, v35, s[40:41]
.LBB0_856:
	v_cvt_pk_bf16_f32 v30, v30, v31
	v_cvt_pk_bf16_f32 v31, v32, v33
	v_cvt_pk_bf16_f32 v32, v26, v27
	v_cvt_pk_bf16_f32 v33, v28, v29
	global_store_dwordx4 v[90:91], v[30:33], off offset:256 sc1
	v_pk_add_f32 v[24:25], v[24:25], v[72:73]
	v_pk_add_f32 v[22:23], v[22:23], v[70:71]
	v_pk_add_f32 v[20:21], v[20:21], v[68:69]
	s_and_b64 vcc, exec, s[42:43]
	v_pk_add_f32 v[18:19], v[18:19], v[66:67]
	s_cbranch_vccnz .LBB0_858
	s_and_b64 vcc, exec, s[40:41]
	s_cbranch_vccnz .Ldyn_dec_14
	v_mul_f32_e32 v22, 0xbfb8aa3b, v22
	v_mul_f32_e32 v18, 0xbfb8aa3b, v18
	v_exp_f32_e32 v22, v22
	v_exp_f32_e32 v18, v18
	v_mul_f32_e32 v23, 0xbfb8aa3b, v23
	v_mul_f32_e32 v19, 0xbfb8aa3b, v19
	v_add_f32_e32 v22, 1.0, v22
	v_add_f32_e32 v18, 1.0, v18
	v_rcp_f32_e32 v22, v22
	v_rcp_f32_e32 v18, v18
	v_exp_f32_e32 v23, v23
	v_exp_f32_e32 v19, v19
	v_add_f32_e32 v23, 1.0, v23
	v_add_f32_e32 v19, 1.0, v19
	v_mul_f32_e32 v24, 0xbfb8aa3b, v24
	v_mul_f32_e32 v20, 0xbfb8aa3b, v20
	v_rcp_f32_e32 v23, v23
	v_rcp_f32_e32 v19, v19
	v_exp_f32_e32 v24, v24
	v_exp_f32_e32 v20, v20
	v_add_f32_e32 v24, 1.0, v24
	v_add_f32_e32 v20, 1.0, v20
	v_mul_f32_e32 v25, 0xbfb8aa3b, v25
	v_mul_f32_e32 v21, 0xbfb8aa3b, v21
	v_rcp_f32_e32 v24, v24
	v_rcp_f32_e32 v20, v20
	v_exp_f32_e32 v25, v25
	v_exp_f32_e32 v21, v21
	v_add_f32_e32 v25, 1.0, v25
	v_add_f32_e32 v21, 1.0, v21
	v_rcp_f32_e32 v25, v25
	v_rcp_f32_e32 v21, v21
	s_branch .LBB0_858
.Ldyn_dec_14:
	v_mul_f32_e32 v22, 0xbfb8aa3b, v22
	v_mul_f32_e32 v18, 0xbfb8aa3b, v18
	v_exp_f32_e32 v22, v22
	v_exp_f32_e32 v18, v18
	v_mul_f32_e32 v23, 0xbfb8aa3b, v23
	v_mul_f32_e32 v19, 0xbfb8aa3b, v19
	v_add_f32_e32 v22, 1.0, v22
	v_add_f32_e32 v18, 1.0, v18
	v_rcp_f32_e32 v22, v22
	v_rcp_f32_e32 v18, v18
	v_exp_f32_e32 v23, v23
	v_exp_f32_e32 v19, v19
	v_mul_f32_e32 v26, 0xbf60028e, v22
	v_mul_f32_e32 v27, 0xbf60028e, v18
	v_add_f32_e32 v23, 1.0, v23
	v_add_f32_e32 v19, 1.0, v19
	v_mul_f32_e32 v24, 0xbfb8aa3b, v24
	v_mul_f32_e32 v20, 0xbfb8aa3b, v20
	v_exp_f32_e32 v26, v26
	v_exp_f32_e32 v27, v27
	v_rcp_f32_e32 v23, v23
	v_rcp_f32_e32 v19, v19
	v_exp_f32_e32 v24, v24
	v_exp_f32_e32 v20, v20
	v_cndmask_b32_e64 v22, v22, v26, s[40:41]
	v_cndmask_b32_e64 v18, v18, v27, s[40:41]
	v_mul_f32_e32 v26, 0xbf60028e, v23
	v_mul_f32_e32 v27, 0xbf60028e, v19
	v_add_f32_e32 v24, 1.0, v24
	v_add_f32_e32 v20, 1.0, v20
	v_mul_f32_e32 v25, 0xbfb8aa3b, v25
	v_mul_f32_e32 v21, 0xbfb8aa3b, v21
	v_exp_f32_e32 v26, v26
	v_exp_f32_e32 v27, v27
	v_rcp_f32_e32 v24, v24
	v_rcp_f32_e32 v20, v20
	v_exp_f32_e32 v25, v25
	v_exp_f32_e32 v21, v21
	v_cndmask_b32_e64 v23, v23, v26, s[40:41]
	v_cndmask_b32_e64 v19, v19, v27, s[40:41]
	v_mul_f32_e32 v26, 0xbf60028e, v24
	v_mul_f32_e32 v27, 0xbf60028e, v20
	v_add_f32_e32 v25, 1.0, v25
	v_add_f32_e32 v21, 1.0, v21
	v_exp_f32_e32 v26, v26
	v_exp_f32_e32 v27, v27
	v_rcp_f32_e32 v25, v25
	v_rcp_f32_e32 v21, v21
	v_cndmask_b32_e64 v24, v24, v26, s[40:41]
	v_cndmask_b32_e64 v20, v20, v27, s[40:41]
	v_mul_f32_e32 v26, 0xbf60028e, v25
	v_mul_f32_e32 v27, 0xbf60028e, v21
	v_exp_f32_e32 v26, v26
	v_exp_f32_e32 v27, v27
	v_cndmask_b32_e64 v25, v25, v26, s[40:41]
	v_cndmask_b32_e64 v21, v21, v27, s[40:41]
.LBB0_858:
	v_cvt_pk_bf16_f32 v22, v22, v23
	v_cvt_pk_bf16_f32 v23, v24, v25
	v_cvt_pk_bf16_f32 v24, v18, v19
	v_cvt_pk_bf16_f32 v25, v20, v21
	global_store_dwordx4 v[82:83], v[22:25], off offset:256 sc1
	v_pk_add_f32 v[16:17], v[16:17], v[72:73]
	v_pk_add_f32 v[14:15], v[14:15], v[70:71]
	v_pk_add_f32 v[12:13], v[12:13], v[68:69]
	s_and_b64 vcc, exec, s[42:43]
	v_pk_add_f32 v[10:11], v[10:11], v[66:67]
	s_cbranch_vccnz .LBB0_860
	s_and_b64 vcc, exec, s[40:41]
	s_cbranch_vccnz .Ldyn_dec_15
	v_mul_f32_e32 v14, 0xbfb8aa3b, v14
	v_mul_f32_e32 v10, 0xbfb8aa3b, v10
	v_exp_f32_e32 v14, v14
	v_exp_f32_e32 v10, v10
	v_mul_f32_e32 v15, 0xbfb8aa3b, v15
	v_mul_f32_e32 v11, 0xbfb8aa3b, v11
	v_add_f32_e32 v14, 1.0, v14
	v_add_f32_e32 v10, 1.0, v10
	v_rcp_f32_e32 v14, v14
	v_rcp_f32_e32 v10, v10
	v_exp_f32_e32 v15, v15
	v_exp_f32_e32 v11, v11
	v_add_f32_e32 v15, 1.0, v15
	v_add_f32_e32 v11, 1.0, v11
	v_mul_f32_e32 v16, 0xbfb8aa3b, v16
	v_mul_f32_e32 v12, 0xbfb8aa3b, v12
	v_rcp_f32_e32 v15, v15
	v_rcp_f32_e32 v11, v11
	v_exp_f32_e32 v16, v16
	v_exp_f32_e32 v12, v12
	v_add_f32_e32 v16, 1.0, v16
	v_add_f32_e32 v12, 1.0, v12
	v_mul_f32_e32 v17, 0xbfb8aa3b, v17
	v_mul_f32_e32 v13, 0xbfb8aa3b, v13
	v_rcp_f32_e32 v16, v16
	v_rcp_f32_e32 v12, v12
	v_exp_f32_e32 v17, v17
	v_exp_f32_e32 v13, v13
	v_add_f32_e32 v17, 1.0, v17
	v_add_f32_e32 v13, 1.0, v13
	v_rcp_f32_e32 v17, v17
	v_rcp_f32_e32 v13, v13
	s_branch .LBB0_860
.Ldyn_dec_15:
	v_mul_f32_e32 v14, 0xbfb8aa3b, v14
	v_mul_f32_e32 v10, 0xbfb8aa3b, v10
	v_exp_f32_e32 v14, v14
	v_exp_f32_e32 v10, v10
	v_mul_f32_e32 v15, 0xbfb8aa3b, v15
	v_mul_f32_e32 v11, 0xbfb8aa3b, v11
	v_add_f32_e32 v14, 1.0, v14
	v_add_f32_e32 v10, 1.0, v10
	v_rcp_f32_e32 v14, v14
	v_rcp_f32_e32 v10, v10
	v_exp_f32_e32 v15, v15
	v_exp_f32_e32 v11, v11
	v_mul_f32_e32 v18, 0xbf60028e, v14
	v_mul_f32_e32 v19, 0xbf60028e, v10
	v_add_f32_e32 v15, 1.0, v15
	v_add_f32_e32 v11, 1.0, v11
	v_mul_f32_e32 v16, 0xbfb8aa3b, v16
	v_mul_f32_e32 v12, 0xbfb8aa3b, v12
	v_exp_f32_e32 v18, v18
	v_exp_f32_e32 v19, v19
	v_rcp_f32_e32 v15, v15
	v_rcp_f32_e32 v11, v11
	v_exp_f32_e32 v16, v16
	v_exp_f32_e32 v12, v12
	v_cndmask_b32_e64 v14, v14, v18, s[40:41]
	v_cndmask_b32_e64 v10, v10, v19, s[40:41]
	v_mul_f32_e32 v18, 0xbf60028e, v15
	v_mul_f32_e32 v19, 0xbf60028e, v11
	v_add_f32_e32 v16, 1.0, v16
	v_add_f32_e32 v12, 1.0, v12
	v_mul_f32_e32 v17, 0xbfb8aa3b, v17
	v_mul_f32_e32 v13, 0xbfb8aa3b, v13
	v_exp_f32_e32 v18, v18
	v_exp_f32_e32 v19, v19
	v_rcp_f32_e32 v16, v16
	v_rcp_f32_e32 v12, v12
	v_exp_f32_e32 v17, v17
	v_exp_f32_e32 v13, v13
	v_cndmask_b32_e64 v15, v15, v18, s[40:41]
	v_cndmask_b32_e64 v11, v11, v19, s[40:41]
	v_mul_f32_e32 v18, 0xbf60028e, v16
	v_mul_f32_e32 v19, 0xbf60028e, v12
	v_add_f32_e32 v17, 1.0, v17
	v_add_f32_e32 v13, 1.0, v13
	v_exp_f32_e32 v18, v18
	v_exp_f32_e32 v19, v19
	v_rcp_f32_e32 v17, v17
	v_rcp_f32_e32 v13, v13
	v_cndmask_b32_e64 v16, v16, v18, s[40:41]
	v_cndmask_b32_e64 v12, v12, v19, s[40:41]
	v_mul_f32_e32 v18, 0xbf60028e, v17
	v_mul_f32_e32 v19, 0xbf60028e, v13
	v_exp_f32_e32 v18, v18
	v_exp_f32_e32 v19, v19
	v_cndmask_b32_e64 v17, v17, v18, s[40:41]
	v_cndmask_b32_e64 v13, v13, v19, s[40:41]
.LBB0_860:
	v_cvt_pk_bf16_f32 v14, v14, v15
	v_cvt_pk_bf16_f32 v15, v16, v17
	v_cvt_pk_bf16_f32 v16, v10, v11
	v_cvt_pk_bf16_f32 v17, v12, v13
	global_store_dwordx4 v[74:75], v[14:17], off offset:256 sc1
	v_pk_add_f32 v[8:9], v[8:9], v[72:73]
	v_pk_add_f32 v[6:7], v[6:7], v[70:71]
	v_pk_add_f32 v[4:5], v[4:5], v[68:69]
	s_and_b64 vcc, exec, s[42:43]
	v_pk_add_f32 v[2:3], v[2:3], v[66:67]
	s_cbranch_vccnz .LBB0_862
	s_and_b64 vcc, exec, s[40:41]
	s_cbranch_vccnz .Ldyn_dec_16
	v_mul_f32_e32 v6, 0xbfb8aa3b, v6
	v_mul_f32_e32 v2, 0xbfb8aa3b, v2
	v_exp_f32_e32 v6, v6
	v_exp_f32_e32 v2, v2
	v_mul_f32_e32 v7, 0xbfb8aa3b, v7
	v_mul_f32_e32 v3, 0xbfb8aa3b, v3
	v_add_f32_e32 v6, 1.0, v6
	v_add_f32_e32 v2, 1.0, v2
	v_rcp_f32_e32 v6, v6
	v_rcp_f32_e32 v2, v2
	v_exp_f32_e32 v7, v7
	v_exp_f32_e32 v3, v3
	v_add_f32_e32 v7, 1.0, v7
	v_add_f32_e32 v3, 1.0, v3
	v_mul_f32_e32 v8, 0xbfb8aa3b, v8
	v_mul_f32_e32 v4, 0xbfb8aa3b, v4
	v_rcp_f32_e32 v7, v7
	v_rcp_f32_e32 v3, v3
	v_exp_f32_e32 v8, v8
	v_exp_f32_e32 v4, v4
	v_add_f32_e32 v8, 1.0, v8
	v_add_f32_e32 v4, 1.0, v4
	v_mul_f32_e32 v9, 0xbfb8aa3b, v9
	v_mul_f32_e32 v5, 0xbfb8aa3b, v5
	v_rcp_f32_e32 v8, v8
	v_rcp_f32_e32 v4, v4
	v_exp_f32_e32 v9, v9
	v_exp_f32_e32 v5, v5
	v_add_f32_e32 v9, 1.0, v9
	v_add_f32_e32 v5, 1.0, v5
	v_rcp_f32_e32 v9, v9
	v_rcp_f32_e32 v5, v5
	s_branch .LBB0_862
.Ldyn_dec_16:
	v_mul_f32_e32 v6, 0xbfb8aa3b, v6
	v_mul_f32_e32 v2, 0xbfb8aa3b, v2
	v_exp_f32_e32 v6, v6
	v_exp_f32_e32 v2, v2
	v_mul_f32_e32 v7, 0xbfb8aa3b, v7
	v_mul_f32_e32 v3, 0xbfb8aa3b, v3
	v_add_f32_e32 v6, 1.0, v6
	v_add_f32_e32 v2, 1.0, v2
	v_rcp_f32_e32 v6, v6
	v_rcp_f32_e32 v2, v2
	v_exp_f32_e32 v7, v7
	v_exp_f32_e32 v3, v3
	v_mul_f32_e32 v10, 0xbf60028e, v6
	v_mul_f32_e32 v11, 0xbf60028e, v2
	v_add_f32_e32 v7, 1.0, v7
	v_add_f32_e32 v3, 1.0, v3
	v_mul_f32_e32 v8, 0xbfb8aa3b, v8
	v_mul_f32_e32 v4, 0xbfb8aa3b, v4
	v_exp_f32_e32 v10, v10
	v_exp_f32_e32 v11, v11
	v_rcp_f32_e32 v7, v7
	v_rcp_f32_e32 v3, v3
	v_exp_f32_e32 v8, v8
	v_exp_f32_e32 v4, v4
	v_cndmask_b32_e64 v6, v6, v10, s[40:41]
	v_cndmask_b32_e64 v2, v2, v11, s[40:41]
	v_mul_f32_e32 v10, 0xbf60028e, v7
	v_mul_f32_e32 v11, 0xbf60028e, v3
	v_add_f32_e32 v8, 1.0, v8
	v_add_f32_e32 v4, 1.0, v4
	v_mul_f32_e32 v9, 0xbfb8aa3b, v9
	v_mul_f32_e32 v5, 0xbfb8aa3b, v5
	v_exp_f32_e32 v10, v10
	v_exp_f32_e32 v11, v11
	v_rcp_f32_e32 v8, v8
	v_rcp_f32_e32 v4, v4
	v_exp_f32_e32 v9, v9
	v_exp_f32_e32 v5, v5
	v_cndmask_b32_e64 v7, v7, v10, s[40:41]
	v_cndmask_b32_e64 v3, v3, v11, s[40:41]
	v_mul_f32_e32 v10, 0xbf60028e, v8
	v_mul_f32_e32 v11, 0xbf60028e, v4
	v_add_f32_e32 v9, 1.0, v9
	v_add_f32_e32 v5, 1.0, v5
	v_exp_f32_e32 v10, v10
	v_exp_f32_e32 v11, v11
	v_rcp_f32_e32 v9, v9
	v_rcp_f32_e32 v5, v5
	v_cndmask_b32_e64 v8, v8, v10, s[40:41]
	v_cndmask_b32_e64 v4, v4, v11, s[40:41]
	v_mul_f32_e32 v10, 0xbf60028e, v9
	v_mul_f32_e32 v11, 0xbf60028e, v5
	v_exp_f32_e32 v10, v10
	v_exp_f32_e32 v11, v11
	v_cndmask_b32_e64 v9, v9, v10, s[40:41]
	v_cndmask_b32_e64 v5, v5, v11, s[40:41]
